# baseline (speedup 1.0000x reference)
.Lmk_start:
	s_mov_b32 s28, s8
	s_mov_b64 s[30:31], s[4:5]
	s_mov_b64 s[32:33], s[6:7]
	s_mov_b64 s[6:7], s[2:3]
	s_mov_b64 s[34:35], s[2:3]
	s_mov_b32 s2, s28
	s_and_b32 s3, s2, 7
	s_lshr_b32 s4, s2, 3
	s_and_b32 s5, s4, 3
	s_lshl_b32 s3, s3, 2
	s_or_b32 s8, s3, s5
	s_lshr_b32 s9, s4, 2
	v_lshrrev_b32_e32 v127, 6, v0
	v_and_b32_e32 v124, 63, v0
	v_lshlrev_b32_e32 v125, 3, v124
	v_lshlrev_b32_e32 v124, 4, v124
	v_readfirstlane_b32 s12, v127
	v_mov_b32_e32 v120, 0
	v_mov_b32_e32 v121, 0
	v_mov_b32_e32 v122, 0
	v_mov_b32_e32 v123, 0
	s_lshl_b32 s13, s12, 10
	s_lshl_b32 s14, s9, 3
	s_add_u32 s14, s14, s12
	s_mul_i32 s15, s14, 0x1800
	s_mul_i32 s16, s8, 0x12000
	s_add_u32 s16, s16, 0xc0000
	s_add_u32 s16, s16, s13
	s_add_u32 s20, s13, 0x2000
	s_add_u32 s10, s6, s16
	s_addc_u32 s11, s7, 0
	s_add_u32 s18, s6, s15
	s_addc_u32 s19, s7, 0
	s_add_u32 s22, s18, 0x1000
	s_addc_u32 s23, s19, 0
	s_cmp_lt_u32 s12, 4
	s_cbranch_scc0 .Lmk_vb
	s_mov_b32 m0, s13
	s_nop 0
	global_load_lds_dwordx4 v124, s[10:11]
	s_add_u32 s26, s10, 0x2000
	s_addc_u32 s27, s11, 0
	s_mov_b32 m0, s20
	s_nop 0
	global_load_lds_dwordx4 v124, s[26:27]
	global_load_dwordx4 v[96:99], v124, s[18:19]
	global_load_dwordx2 v[100:101], v125, s[22:23]
	global_load_dwordx4 v[102:105], v124, s[18:19] offset:1024
	global_load_dwordx2 v[106:107], v125, s[22:23] offset:512
	global_load_dwordx4 v[108:111], v124, s[18:19] offset:2048
	global_load_dwordx2 v[112:113], v125, s[22:23] offset:1024
	global_load_dwordx4 v[114:117], v124, s[18:19] offset:3072
	global_load_dwordx2 v[118:119], v125, s[22:23] offset:1536
	s_add_u32 s24, s10, 0x3000
	s_addc_u32 s25, s11, 0
	s_add_u32 s26, s13, 0x3000
	s_mov_b32 m0, s26
	s_nop 0
	global_load_lds_dwordx4 v124, s[24:25]
	s_add_u32 s26, s24, 0x2000
	s_addc_u32 s27, s25, 0
	s_add_u32 s29, s20, 0x3000
	s_mov_b32 m0, s29
	s_nop 0
	global_load_lds_dwordx4 v124, s[26:27]
	s_add_u32 s24, s10, 0x6000
	s_addc_u32 s25, s11, 0
	s_add_u32 s26, s13, 0x6000
	s_mov_b32 m0, s26
	s_nop 0
	global_load_lds_dwordx4 v124, s[24:25]
	s_add_u32 s26, s24, 0x2000
	s_addc_u32 s27, s25, 0
	s_add_u32 s29, s20, 0x6000
	s_mov_b32 m0, s29
	s_nop 0
	global_load_lds_dwordx4 v124, s[26:27]
	s_add_u32 s24, s10, 0x9000
	s_addc_u32 s25, s11, 0
	s_add_u32 s26, s13, 0x9000
	s_mov_b32 m0, s26
	s_nop 0
	global_load_lds_dwordx4 v124, s[24:25]
	s_add_u32 s26, s24, 0x2000
	s_addc_u32 s27, s25, 0
	s_add_u32 s29, s20, 0x9000
	s_mov_b32 m0, s29
	s_nop 0
	global_load_lds_dwordx4 v124, s[26:27]
	s_add_u32 s24, s10, 0xc000
	s_addc_u32 s25, s11, 0
	s_add_u32 s26, s13, 0xc000
	s_mov_b32 m0, s26
	s_nop 0
	global_load_lds_dwordx4 v124, s[24:25]
	s_add_u32 s26, s24, 0x2000
	s_addc_u32 s27, s25, 0
	s_add_u32 s29, s20, 0xc000
	s_mov_b32 m0, s29
	s_nop 0
	global_load_lds_dwordx4 v124, s[26:27]
	s_waitcnt vmcnt(8)
	s_barrier
	ds_read_b128 v[0:3], v124
	ds_read_b64 v[4:5], v125 offset:4096
	ds_read_b128 v[6:9], v124 offset:1024
	ds_read_b64 v[10:11], v125 offset:4608
	ds_read_b128 v[12:15], v124 offset:2048
	ds_read_b64 v[16:17], v125 offset:5120
	ds_read_b128 v[18:21], v124 offset:3072
	ds_read_b64 v[22:23], v125 offset:5632
	s_waitcnt lgkmcnt(0)
	s_setprio 2
	s_nop 0
	v_mfma_f32_32x32x64_f8f6f4 v[48:63], v[0:5], v[96:101], 0 cbsz:2 blgp:2
	ds_read_b128 v[24:27], v124 offset:6144
	ds_read_b64 v[28:29], v125 offset:10240
	v_mfma_f32_32x32x64_f8f6f4 v[48:63], v[6:11], v[102:107], v[48:63] cbsz:2 blgp:2
	ds_read_b128 v[30:33], v124 offset:7168
	ds_read_b64 v[34:35], v125 offset:10752
	v_mfma_f32_32x32x64_f8f6f4 v[48:63], v[12:17], v[108:113], v[48:63] cbsz:2 blgp:2
	ds_read_b128 v[36:39], v124 offset:8192
	ds_read_b64 v[40:41], v125 offset:11264
	v_mfma_f32_32x32x64_f8f6f4 v[48:63], v[18:23], v[114:119], v[48:63] cbsz:2 blgp:2
	ds_read_b128 v[42:45], v124 offset:9216
	ds_read_b64 v[46:47], v125 offset:11776
	s_waitcnt vmcnt(6) lgkmcnt(0)
	s_barrier
	s_add_u32 s24, s10, 0xf000
	s_addc_u32 s25, s11, 0
	s_mov_b32 m0, s13
	s_nop 0
	global_load_lds_dwordx4 v124, s[24:25]
	s_add_u32 s26, s24, 0x2000
	s_addc_u32 s27, s25, 0
	s_mov_b32 m0, s20
	s_nop 0
	global_load_lds_dwordx4 v124, s[26:27]
	v_mfma_f32_32x32x64_f8f6f4 v[64:79], v[24:29], v[96:101], 0 cbsz:2 blgp:2
	ds_read_b128 v[0:3], v124 offset:12288
	ds_read_b64 v[4:5], v125 offset:16384
	ds_read_b128 v[6:9], v124 offset:13312
	ds_read_b64 v[10:11], v125 offset:16896
	ds_read_b128 v[24:27], v124 offset:18432
	ds_read_b64 v[28:29], v125 offset:22528
	v_mfma_f32_32x32x64_f8f6f4 v[64:79], v[30:35], v[102:107], v[64:79] cbsz:2 blgp:2
	ds_read_b128 v[12:15], v124 offset:14336
	ds_read_b64 v[16:17], v125 offset:17408
	ds_read_b128 v[18:21], v124 offset:15360
	ds_read_b64 v[22:23], v125 offset:17920
	ds_read_b128 v[30:33], v124 offset:19456
	ds_read_b64 v[34:35], v125 offset:23040
	v_exp_f32_e32 v48, v48
	v_exp_f32_e32 v49, v49
	v_exp_f32_e32 v50, v50
	v_exp_f32_e32 v51, v51
	v_mfma_f32_32x32x64_f8f6f4 v[64:79], v[36:41], v[108:113], v[64:79] cbsz:2 blgp:2
	ds_read_b128 v[36:39], v124 offset:20480
	ds_read_b64 v[40:41], v125 offset:23552
	v_exp_f32_e32 v52, v52
	v_exp_f32_e32 v53, v53
	v_exp_f32_e32 v54, v54
	v_exp_f32_e32 v55, v55
	v_pk_add_f32 v[120:121], v[120:121], v[48:49]
	v_pk_add_f32 v[122:123], v[122:123], v[50:51]
	v_mfma_f32_32x32x64_f8f6f4 v[64:79], v[42:47], v[114:119], v[64:79] cbsz:2 blgp:2
	ds_read_b128 v[42:45], v124 offset:21504
	ds_read_b64 v[46:47], v125 offset:24064
	v_exp_f32_e32 v56, v56
	v_exp_f32_e32 v57, v57
	v_exp_f32_e32 v58, v58
	v_exp_f32_e32 v59, v59
	v_pk_add_f32 v[120:121], v[120:121], v[52:53]
	v_pk_add_f32 v[122:123], v[122:123], v[54:55]
	s_waitcnt vmcnt(6) lgkmcnt(6)
	s_barrier
	v_mfma_f32_32x32x64_f8f6f4 v[80:95], v[0:5], v[96:101], 0 cbsz:2 blgp:2
	ds_read_b128 v[0:3], v124 offset:24576
	ds_read_b64 v[4:5], v125 offset:28672
	v_exp_f32_e32 v60, v60
	v_exp_f32_e32 v61, v61
	v_exp_f32_e32 v62, v62
	v_exp_f32_e32 v63, v63
	v_pk_add_f32 v[120:121], v[120:121], v[56:57]
	v_pk_add_f32 v[122:123], v[122:123], v[58:59]
	v_mfma_f32_32x32x64_f8f6f4 v[80:95], v[6:11], v[102:107], v[80:95] cbsz:2 blgp:2
	ds_read_b128 v[6:9], v124 offset:25600
	ds_read_b64 v[10:11], v125 offset:29184
	v_exp_f32_e32 v64, v64
	v_exp_f32_e32 v65, v65
	v_exp_f32_e32 v66, v66
	v_exp_f32_e32 v67, v67
	v_pk_add_f32 v[120:121], v[120:121], v[60:61]
	v_pk_add_f32 v[122:123], v[122:123], v[62:63]
	v_mfma_f32_32x32x64_f8f6f4 v[80:95], v[12:17], v[108:113], v[80:95] cbsz:2 blgp:2
	ds_read_b128 v[12:15], v124 offset:26624
	ds_read_b64 v[16:17], v125 offset:29696
	v_exp_f32_e32 v68, v68
	v_exp_f32_e32 v69, v69
	v_exp_f32_e32 v70, v70
	v_exp_f32_e32 v71, v71
	v_pk_add_f32 v[120:121], v[120:121], v[64:65]
	v_pk_add_f32 v[122:123], v[122:123], v[66:67]
	v_mfma_f32_32x32x64_f8f6f4 v[80:95], v[18:23], v[114:119], v[80:95] cbsz:2 blgp:2
	ds_read_b128 v[18:21], v124 offset:27648
	ds_read_b64 v[22:23], v125 offset:30208
	v_exp_f32_e32 v72, v72
	v_exp_f32_e32 v73, v73
	v_exp_f32_e32 v74, v74
	v_exp_f32_e32 v75, v75
	v_pk_add_f32 v[120:121], v[120:121], v[68:69]
	v_pk_add_f32 v[122:123], v[122:123], v[70:71]
	s_waitcnt lgkmcnt(8)
	s_nop 0
	v_mfma_f32_32x32x64_f8f6f4 v[48:63], v[24:29], v[96:101], 0 cbsz:2 blgp:2
	ds_read_b128 v[24:27], v124 offset:30720
	ds_read_b64 v[28:29], v125 offset:34816
	v_exp_f32_e32 v76, v76
	v_exp_f32_e32 v77, v77
	v_exp_f32_e32 v78, v78
	v_exp_f32_e32 v79, v79
	v_pk_add_f32 v[120:121], v[120:121], v[72:73]
	v_pk_add_f32 v[122:123], v[122:123], v[74:75]
	v_mfma_f32_32x32x64_f8f6f4 v[48:63], v[30:35], v[102:107], v[48:63] cbsz:2 blgp:2
	ds_read_b128 v[30:33], v124 offset:31744
	ds_read_b64 v[34:35], v125 offset:35328
	v_exp_f32_e32 v80, v80
	v_exp_f32_e32 v81, v81
	v_exp_f32_e32 v82, v82
	v_exp_f32_e32 v83, v83
	v_pk_add_f32 v[120:121], v[120:121], v[76:77]
	v_pk_add_f32 v[122:123], v[122:123], v[78:79]
	v_mfma_f32_32x32x64_f8f6f4 v[48:63], v[36:41], v[108:113], v[48:63] cbsz:2 blgp:2
	ds_read_b128 v[36:39], v124 offset:32768
	ds_read_b64 v[40:41], v125 offset:35840
	v_exp_f32_e32 v84, v84
	v_exp_f32_e32 v85, v85
	v_exp_f32_e32 v86, v86
	v_exp_f32_e32 v87, v87
	v_pk_add_f32 v[120:121], v[120:121], v[80:81]
	v_pk_add_f32 v[122:123], v[122:123], v[82:83]
	v_mfma_f32_32x32x64_f8f6f4 v[48:63], v[42:47], v[114:119], v[48:63] cbsz:2 blgp:2
	ds_read_b128 v[42:45], v124 offset:33792
	ds_read_b64 v[46:47], v125 offset:36352
	v_exp_f32_e32 v88, v88
	v_exp_f32_e32 v89, v89
	v_exp_f32_e32 v90, v90
	v_exp_f32_e32 v91, v91
	v_pk_add_f32 v[120:121], v[120:121], v[84:85]
	v_pk_add_f32 v[122:123], v[122:123], v[86:87]
	s_setprio 1
	s_waitcnt vmcnt(4) lgkmcnt(8)
	s_barrier
	s_nop 0
	v_mfma_f32_32x32x64_f8f6f4 v[64:79], v[0:5], v[96:101], 0 cbsz:2 blgp:2
	ds_read_b128 v[0:3], v124 offset:36864
	ds_read_b64 v[4:5], v125 offset:40960
	v_exp_f32_e32 v92, v92
	v_exp_f32_e32 v93, v93
	v_exp_f32_e32 v94, v94
	v_exp_f32_e32 v95, v95
	v_pk_add_f32 v[120:121], v[120:121], v[88:89]
	v_pk_add_f32 v[122:123], v[122:123], v[90:91]
	v_mfma_f32_32x32x64_f8f6f4 v[64:79], v[6:11], v[102:107], v[64:79] cbsz:2 blgp:2
	ds_read_b128 v[6:9], v124 offset:37888
	ds_read_b64 v[10:11], v125 offset:41472
	v_exp_f32_e32 v48, v48
	v_exp_f32_e32 v49, v49
	v_exp_f32_e32 v50, v50
	v_exp_f32_e32 v51, v51
	v_pk_add_f32 v[120:121], v[120:121], v[92:93]
	v_pk_add_f32 v[122:123], v[122:123], v[94:95]
	v_mfma_f32_32x32x64_f8f6f4 v[64:79], v[12:17], v[108:113], v[64:79] cbsz:2 blgp:2
	ds_read_b128 v[12:15], v124 offset:38912
	ds_read_b64 v[16:17], v125 offset:41984
	v_exp_f32_e32 v52, v52
	v_exp_f32_e32 v53, v53
	v_exp_f32_e32 v54, v54
	v_exp_f32_e32 v55, v55
	v_pk_add_f32 v[120:121], v[120:121], v[48:49]
	v_pk_add_f32 v[122:123], v[122:123], v[50:51]
	v_mfma_f32_32x32x64_f8f6f4 v[64:79], v[18:23], v[114:119], v[64:79] cbsz:2 blgp:2
	ds_read_b128 v[18:21], v124 offset:39936
	ds_read_b64 v[22:23], v125 offset:42496
	v_exp_f32_e32 v56, v56
	v_exp_f32_e32 v57, v57
	v_exp_f32_e32 v58, v58
	v_exp_f32_e32 v59, v59
	v_pk_add_f32 v[120:121], v[120:121], v[52:53]
	v_pk_add_f32 v[122:123], v[122:123], v[54:55]
	s_waitcnt lgkmcnt(8)
	s_nop 0
	v_mfma_f32_32x32x64_f8f6f4 v[80:95], v[24:29], v[96:101], 0 cbsz:2 blgp:2
	ds_read_b128 v[24:27], v124 offset:43008
	ds_read_b64 v[28:29], v125 offset:47104
	v_exp_f32_e32 v60, v60
	v_exp_f32_e32 v61, v61
	v_exp_f32_e32 v62, v62
	v_exp_f32_e32 v63, v63
	v_pk_add_f32 v[120:121], v[120:121], v[56:57]
	v_pk_add_f32 v[122:123], v[122:123], v[58:59]
	v_mfma_f32_32x32x64_f8f6f4 v[80:95], v[30:35], v[102:107], v[80:95] cbsz:2 blgp:2
	ds_read_b128 v[30:33], v124 offset:44032
	ds_read_b64 v[34:35], v125 offset:47616
	v_exp_f32_e32 v64, v64
	v_exp_f32_e32 v65, v65
	v_exp_f32_e32 v66, v66
	v_exp_f32_e32 v67, v67
	v_pk_add_f32 v[120:121], v[120:121], v[60:61]
	v_pk_add_f32 v[122:123], v[122:123], v[62:63]
	v_mfma_f32_32x32x64_f8f6f4 v[80:95], v[36:41], v[108:113], v[80:95] cbsz:2 blgp:2
	ds_read_b128 v[36:39], v124 offset:45056
	ds_read_b64 v[40:41], v125 offset:48128
	v_exp_f32_e32 v68, v68
	v_exp_f32_e32 v69, v69
	v_exp_f32_e32 v70, v70
	v_exp_f32_e32 v71, v71
	v_pk_add_f32 v[120:121], v[120:121], v[64:65]
	v_pk_add_f32 v[122:123], v[122:123], v[66:67]
	v_mfma_f32_32x32x64_f8f6f4 v[80:95], v[42:47], v[114:119], v[80:95] cbsz:2 blgp:2
	ds_read_b128 v[42:45], v124 offset:46080
	ds_read_b64 v[46:47], v125 offset:48640
	v_exp_f32_e32 v72, v72
	v_exp_f32_e32 v73, v73
	v_exp_f32_e32 v74, v74
	v_exp_f32_e32 v75, v75
	v_pk_add_f32 v[120:121], v[120:121], v[68:69]
	v_pk_add_f32 v[122:123], v[122:123], v[70:71]
	s_waitcnt vmcnt(2) lgkmcnt(8)
	s_barrier
	v_mfma_f32_32x32x64_f8f6f4 v[48:63], v[0:5], v[96:101], 0 cbsz:2 blgp:2
	ds_read_b128 v[0:3], v124 offset:49152
	ds_read_b64 v[4:5], v125 offset:53248
	v_exp_f32_e32 v76, v76
	v_exp_f32_e32 v77, v77
	v_exp_f32_e32 v78, v78
	v_exp_f32_e32 v79, v79
	v_pk_add_f32 v[120:121], v[120:121], v[72:73]
	v_pk_add_f32 v[122:123], v[122:123], v[74:75]
	v_mfma_f32_32x32x64_f8f6f4 v[48:63], v[6:11], v[102:107], v[48:63] cbsz:2 blgp:2
	ds_read_b128 v[6:9], v124 offset:50176
	ds_read_b64 v[10:11], v125 offset:53760
	v_exp_f32_e32 v80, v80
	v_exp_f32_e32 v81, v81
	v_exp_f32_e32 v82, v82
	v_exp_f32_e32 v83, v83
	v_pk_add_f32 v[120:121], v[120:121], v[76:77]
	v_pk_add_f32 v[122:123], v[122:123], v[78:79]
	v_mfma_f32_32x32x64_f8f6f4 v[48:63], v[12:17], v[108:113], v[48:63] cbsz:2 blgp:2
	ds_read_b128 v[12:15], v124 offset:51200
	ds_read_b64 v[16:17], v125 offset:54272
	v_exp_f32_e32 v84, v84
	v_exp_f32_e32 v85, v85
	v_exp_f32_e32 v86, v86
	v_exp_f32_e32 v87, v87
	v_pk_add_f32 v[120:121], v[120:121], v[80:81]
	v_pk_add_f32 v[122:123], v[122:123], v[82:83]
	v_mfma_f32_32x32x64_f8f6f4 v[48:63], v[18:23], v[114:119], v[48:63] cbsz:2 blgp:2
	ds_read_b128 v[18:21], v124 offset:52224
	ds_read_b64 v[22:23], v125 offset:54784
	v_exp_f32_e32 v88, v88
	v_exp_f32_e32 v89, v89
	v_exp_f32_e32 v90, v90
	v_exp_f32_e32 v91, v91
	v_pk_add_f32 v[120:121], v[120:121], v[84:85]
	v_pk_add_f32 v[122:123], v[122:123], v[86:87]
	s_waitcnt lgkmcnt(8)
	s_nop 0
	v_mfma_f32_32x32x64_f8f6f4 v[64:79], v[24:29], v[96:101], 0 cbsz:2 blgp:2
	ds_read_b128 v[24:27], v124 offset:55296
	ds_read_b64 v[28:29], v125 offset:59392
	v_exp_f32_e32 v92, v92
	v_exp_f32_e32 v93, v93
	v_exp_f32_e32 v94, v94
	v_exp_f32_e32 v95, v95
	v_pk_add_f32 v[120:121], v[120:121], v[88:89]
	v_pk_add_f32 v[122:123], v[122:123], v[90:91]
	v_mfma_f32_32x32x64_f8f6f4 v[64:79], v[30:35], v[102:107], v[64:79] cbsz:2 blgp:2
	ds_read_b128 v[30:33], v124 offset:56320
	ds_read_b64 v[34:35], v125 offset:59904
	v_exp_f32_e32 v48, v48
	v_exp_f32_e32 v49, v49
	v_exp_f32_e32 v50, v50
	v_exp_f32_e32 v51, v51
	v_pk_add_f32 v[120:121], v[120:121], v[92:93]
	v_pk_add_f32 v[122:123], v[122:123], v[94:95]
	v_mfma_f32_32x32x64_f8f6f4 v[64:79], v[36:41], v[108:113], v[64:79] cbsz:2 blgp:2
	ds_read_b128 v[36:39], v124 offset:57344
	ds_read_b64 v[40:41], v125 offset:60416
	v_exp_f32_e32 v52, v52
	v_exp_f32_e32 v53, v53
	v_exp_f32_e32 v54, v54
	v_exp_f32_e32 v55, v55
	v_pk_add_f32 v[120:121], v[120:121], v[48:49]
	v_pk_add_f32 v[122:123], v[122:123], v[50:51]
	v_mfma_f32_32x32x64_f8f6f4 v[64:79], v[42:47], v[114:119], v[64:79] cbsz:2 blgp:2
	ds_read_b128 v[42:45], v124 offset:58368
	ds_read_b64 v[46:47], v125 offset:60928
	v_exp_f32_e32 v56, v56
	v_exp_f32_e32 v57, v57
	v_exp_f32_e32 v58, v58
	v_exp_f32_e32 v59, v59
	v_pk_add_f32 v[120:121], v[120:121], v[52:53]
	v_pk_add_f32 v[122:123], v[122:123], v[54:55]
	s_setprio 0
	s_waitcnt vmcnt(0) lgkmcnt(8)
	s_barrier
	s_nop 0
	v_mfma_f32_32x32x64_f8f6f4 v[80:95], v[0:5], v[96:101], 0 cbsz:2 blgp:2
	ds_read_b128 v[0:3], v124
	ds_read_b64 v[4:5], v125 offset:4096
	v_exp_f32_e32 v60, v60
	v_exp_f32_e32 v61, v61
	v_exp_f32_e32 v62, v62
	v_exp_f32_e32 v63, v63
	v_pk_add_f32 v[120:121], v[120:121], v[56:57]
	v_pk_add_f32 v[122:123], v[122:123], v[58:59]
	v_mfma_f32_32x32x64_f8f6f4 v[80:95], v[6:11], v[102:107], v[80:95] cbsz:2 blgp:2
	ds_read_b128 v[6:9], v124 offset:1024
	ds_read_b64 v[10:11], v125 offset:4608
	v_exp_f32_e32 v64, v64
	v_exp_f32_e32 v65, v65
	v_exp_f32_e32 v66, v66
	v_exp_f32_e32 v67, v67
	v_pk_add_f32 v[120:121], v[120:121], v[60:61]
	v_pk_add_f32 v[122:123], v[122:123], v[62:63]
	v_mfma_f32_32x32x64_f8f6f4 v[80:95], v[12:17], v[108:113], v[80:95] cbsz:2 blgp:2
	ds_read_b128 v[12:15], v124 offset:2048
	ds_read_b64 v[16:17], v125 offset:5120
	v_exp_f32_e32 v68, v68
	v_exp_f32_e32 v69, v69
	v_exp_f32_e32 v70, v70
	v_exp_f32_e32 v71, v71
	v_pk_add_f32 v[120:121], v[120:121], v[64:65]
	v_pk_add_f32 v[122:123], v[122:123], v[66:67]
	v_mfma_f32_32x32x64_f8f6f4 v[80:95], v[18:23], v[114:119], v[80:95] cbsz:2 blgp:2
	ds_read_b128 v[18:21], v124 offset:3072
	ds_read_b64 v[22:23], v125 offset:5632
	v_exp_f32_e32 v72, v72
	v_exp_f32_e32 v73, v73
	v_exp_f32_e32 v74, v74
	v_exp_f32_e32 v75, v75
	v_pk_add_f32 v[120:121], v[120:121], v[68:69]
	v_pk_add_f32 v[122:123], v[122:123], v[70:71]
	s_waitcnt lgkmcnt(8)
	s_nop 0
	v_mfma_f32_32x32x64_f8f6f4 v[48:63], v[24:29], v[96:101], 0 cbsz:2 blgp:2
	ds_read_b128 v[24:27], v124 offset:6144
	ds_read_b64 v[28:29], v125 offset:10240
	v_exp_f32_e32 v76, v76
	v_exp_f32_e32 v77, v77
	v_exp_f32_e32 v78, v78
	v_exp_f32_e32 v79, v79
	v_pk_add_f32 v[120:121], v[120:121], v[72:73]
	v_pk_add_f32 v[122:123], v[122:123], v[74:75]
	v_mfma_f32_32x32x64_f8f6f4 v[48:63], v[30:35], v[102:107], v[48:63] cbsz:2 blgp:2
	ds_read_b128 v[30:33], v124 offset:7168
	ds_read_b64 v[34:35], v125 offset:10752
	v_exp_f32_e32 v80, v80
	v_exp_f32_e32 v81, v81
	v_exp_f32_e32 v82, v82
	v_exp_f32_e32 v83, v83
	v_pk_add_f32 v[120:121], v[120:121], v[76:77]
	v_pk_add_f32 v[122:123], v[122:123], v[78:79]
	s_cmp_lg_u32 s8, 10
	s_cbranch_scc1 .Lmk_nosplit_a
	v_add_f32_e32 v127, v120, v121
	v_add_f32_e32 v126, v122, v123
	v_mov_b32_e32 v120, 0
	v_mov_b32_e32 v121, 0
	v_mov_b32_e32 v122, 0
	v_mov_b32_e32 v123, 0
	v_add_f32_e32 v127, v127, v126
.Lmk_nosplit_a:
	s_nop 0
	v_mfma_f32_32x32x64_f8f6f4 v[48:63], v[36:41], v[108:113], v[48:63] cbsz:2 blgp:2
	ds_read_b128 v[36:39], v124 offset:8192
	ds_read_b64 v[40:41], v125 offset:11264
	v_exp_f32_e32 v84, v84
	v_exp_f32_e32 v85, v85
	v_exp_f32_e32 v86, v86
	v_exp_f32_e32 v87, v87
	v_pk_add_f32 v[120:121], v[120:121], v[80:81]
	v_pk_add_f32 v[122:123], v[122:123], v[82:83]
	v_mfma_f32_32x32x64_f8f6f4 v[48:63], v[42:47], v[114:119], v[48:63] cbsz:2 blgp:2
	ds_read_b128 v[42:45], v124 offset:9216
	ds_read_b64 v[46:47], v125 offset:11776
	v_exp_f32_e32 v88, v88
	v_exp_f32_e32 v89, v89
	v_exp_f32_e32 v90, v90
	v_exp_f32_e32 v91, v91
	v_pk_add_f32 v[120:121], v[120:121], v[84:85]
	v_pk_add_f32 v[122:123], v[122:123], v[86:87]
	s_waitcnt lgkmcnt(8)
	s_nop 0
	v_mfma_f32_32x32x64_f8f6f4 v[64:79], v[0:5], v[96:101], 0 cbsz:2 blgp:2
	v_exp_f32_e32 v92, v92
	v_exp_f32_e32 v93, v93
	v_exp_f32_e32 v94, v94
	v_exp_f32_e32 v95, v95
	v_pk_add_f32 v[120:121], v[120:121], v[88:89]
	v_pk_add_f32 v[122:123], v[122:123], v[90:91]
	v_mfma_f32_32x32x64_f8f6f4 v[64:79], v[6:11], v[102:107], v[64:79] cbsz:2 blgp:2
	v_exp_f32_e32 v48, v48
	v_exp_f32_e32 v49, v49
	v_exp_f32_e32 v50, v50
	v_exp_f32_e32 v51, v51
	v_pk_add_f32 v[120:121], v[120:121], v[92:93]
	v_pk_add_f32 v[122:123], v[122:123], v[94:95]
	v_mfma_f32_32x32x64_f8f6f4 v[64:79], v[12:17], v[108:113], v[64:79] cbsz:2 blgp:2
	v_exp_f32_e32 v52, v52
	v_exp_f32_e32 v53, v53
	v_exp_f32_e32 v54, v54
	v_exp_f32_e32 v55, v55
	v_pk_add_f32 v[120:121], v[120:121], v[48:49]
	v_pk_add_f32 v[122:123], v[122:123], v[50:51]
	v_mfma_f32_32x32x64_f8f6f4 v[64:79], v[18:23], v[114:119], v[64:79] cbsz:2 blgp:2
	v_exp_f32_e32 v56, v56
	v_exp_f32_e32 v57, v57
	v_exp_f32_e32 v58, v58
	v_exp_f32_e32 v59, v59
	v_pk_add_f32 v[120:121], v[120:121], v[52:53]
	v_pk_add_f32 v[122:123], v[122:123], v[54:55]
	s_waitcnt lgkmcnt(0)
	s_nop 0
	v_mfma_f32_32x32x64_f8f6f4 v[80:95], v[24:29], v[96:101], 0 cbsz:2 blgp:2
	v_exp_f32_e32 v60, v60
	v_exp_f32_e32 v61, v61
	v_exp_f32_e32 v62, v62
	v_exp_f32_e32 v63, v63
	v_pk_add_f32 v[120:121], v[120:121], v[56:57]
	v_pk_add_f32 v[122:123], v[122:123], v[58:59]
	v_mfma_f32_32x32x64_f8f6f4 v[80:95], v[30:35], v[102:107], v[80:95] cbsz:2 blgp:2
	v_exp_f32_e32 v64, v64
	v_exp_f32_e32 v65, v65
	v_exp_f32_e32 v66, v66
	v_exp_f32_e32 v67, v67
	v_pk_add_f32 v[120:121], v[120:121], v[60:61]
	v_pk_add_f32 v[122:123], v[122:123], v[62:63]
	v_mfma_f32_32x32x64_f8f6f4 v[80:95], v[36:41], v[108:113], v[80:95] cbsz:2 blgp:2
	v_exp_f32_e32 v68, v68
	v_exp_f32_e32 v69, v69
	v_exp_f32_e32 v70, v70
	v_exp_f32_e32 v71, v71
	v_pk_add_f32 v[120:121], v[120:121], v[64:65]
	v_pk_add_f32 v[122:123], v[122:123], v[66:67]
	v_mfma_f32_32x32x64_f8f6f4 v[80:95], v[42:47], v[114:119], v[80:95] cbsz:2 blgp:2
	v_exp_f32_e32 v72, v72
	v_exp_f32_e32 v73, v73
	v_exp_f32_e32 v74, v74
	v_exp_f32_e32 v75, v75
	v_pk_add_f32 v[120:121], v[120:121], v[68:69]
	v_pk_add_f32 v[122:123], v[122:123], v[70:71]
	v_exp_f32_e32 v76, v76
	v_exp_f32_e32 v77, v77
	v_exp_f32_e32 v78, v78
	v_exp_f32_e32 v79, v79
	v_pk_add_f32 v[120:121], v[120:121], v[72:73]
	v_pk_add_f32 v[122:123], v[122:123], v[74:75]
	s_nop 1
	v_exp_f32_e32 v80, v80
	v_exp_f32_e32 v81, v81
	v_exp_f32_e32 v82, v82
	v_exp_f32_e32 v83, v83
	v_pk_add_f32 v[120:121], v[120:121], v[76:77]
	v_pk_add_f32 v[122:123], v[122:123], v[78:79]
	v_exp_f32_e32 v84, v84
	v_exp_f32_e32 v85, v85
	v_exp_f32_e32 v86, v86
	v_exp_f32_e32 v87, v87
	v_pk_add_f32 v[120:121], v[120:121], v[80:81]
	v_pk_add_f32 v[122:123], v[122:123], v[82:83]
	v_exp_f32_e32 v88, v88
	v_exp_f32_e32 v89, v89
	v_exp_f32_e32 v90, v90
	v_exp_f32_e32 v91, v91
	v_pk_add_f32 v[120:121], v[120:121], v[84:85]
	v_pk_add_f32 v[122:123], v[122:123], v[86:87]
	v_exp_f32_e32 v92, v92
	v_exp_f32_e32 v93, v93
	v_exp_f32_e32 v94, v94
	v_exp_f32_e32 v95, v95
	v_pk_add_f32 v[120:121], v[120:121], v[88:89]
	v_pk_add_f32 v[122:123], v[122:123], v[90:91]
	v_pk_add_f32 v[120:121], v[120:121], v[92:93]
	v_pk_add_f32 v[122:123], v[122:123], v[94:95]
	v_add_f32_e32 v120, v120, v121
	v_add_f32_e32 v122, v122, v123
	v_lshrrev_b32_e32 v126, 2, v124
	v_add_f32_e32 v120, v120, v122
	v_xor_b32_e32 v125, 0x80, v126
	s_mov_b64 s[4:5], s[30:31]
	s_mov_b64 s[6:7], s[32:33]
	ds_bpermute_b32 v122, v125, v120
	ds_bpermute_b32 v123, v125, v127
	s_lshl_b32 s14, s14, 7
	v_add_u32_e32 v126, s14, v126
	v_cmp_gt_u32_e32 vcc, 0x200, v124
	s_and_saveexec_b64 s[16:17], vcc
	s_cbranch_execz .Lmk_end_a
	s_waitcnt lgkmcnt(0)
	v_add_f32_e32 v120, v120, v122
	v_add_f32_e32 v127, v127, v123
	s_cmp_lt_u32 s8, 10
	s_cbranch_scc1 .Lmk_pos_only_a
	s_cmp_eq_u32 s8, 10
	s_cbranch_scc0 .Lmk_neg_only_a
	global_atomic_add_f32 v126, v127, s[4:5]
